# speedup vs baseline: 1.0428x; 1.0045x over previous
.LBB2_63:
	s_or_b64 exec, exec, s[40:41]
	s_waitcnt vmcnt(0)
	v_lshl_add_u64 v[10:11], v[64:65], 0, s[30:31]
	v_lshl_add_u64 v[12:13], v[62:63], 0, s[30:31]
	v_lshl_add_u64 v[46:47], v[60:61], 0, s[30:31]
	s_waitcnt lgkmcnt(0)
	s_barrier
	global_load_dwordx4 v[34:37], v[10:11], off
	global_load_dwordx4 v[30:33], v[12:13], off
	v_lshl_add_u64 v[48:49], v[58:59], 0, s[30:31]
	global_load_dwordx4 v[26:29], v[46:47], off
	global_load_dwordx4 v[22:25], v[48:49], off
	global_load_dwordx4 v[18:21], v[56:57], off
	global_load_dwordx4 v[14:17], v[0:1], off
	global_load_dwordx4 v[10:13], v[54:55], off
	s_and_b64 vcc, exec, s[6:7]
	s_cbranch_vccnz .Lht_t1
	ds_read_b128 v[90:93], v70 offset:29568
	ds_read_b128 v[46:49], v79
	ds_read_b128 v[50:53], v79 offset:1024
	ds_read_b128 v[94:97], v70 offset:30592
	ds_read_b128 v[106:109], v70 offset:31616
	ds_read_b128 v[98:101], v78
	ds_read_b128 v[102:105], v78 offset:1024
	ds_read_b128 v[110:113], v70 offset:32640
	s_waitcnt lgkmcnt(4)
	v_mfma_f32_16x16x32_f16 v[42:45], v[90:93], v[46:49], v[42:45]
	v_mfma_f32_16x16x32_f16 v[38:41], v[90:93], v[50:53], v[38:41]
	v_mfma_f32_16x16x32_f16 v[6:9], v[94:97], v[46:49], v[6:9]
	v_mfma_f32_16x16x32_f16 v[2:5], v[94:97], v[50:53], v[2:5]
	ds_read_b128 v[90:93], v70 offset:33664
	ds_read_b128 v[46:49], v77
	ds_read_b128 v[50:53], v77 offset:1024
	ds_read_b128 v[94:97], v70 offset:34688
	s_waitcnt lgkmcnt(4)
	v_mfma_f32_16x16x32_f16 v[42:45], v[106:109], v[98:101], v[42:45]
	v_mfma_f32_16x16x32_f16 v[38:41], v[106:109], v[102:105], v[38:41]
	v_mfma_f32_16x16x32_f16 v[6:9], v[110:113], v[98:101], v[6:9]
	v_mfma_f32_16x16x32_f16 v[2:5], v[110:113], v[102:105], v[2:5]
	ds_read_b128 v[106:109], v70 offset:35712
	ds_read_b128 v[98:101], v76
	ds_read_b128 v[102:105], v76 offset:1024
	ds_read_b128 v[110:113], v70 offset:36736
	s_waitcnt lgkmcnt(4)
	v_mfma_f32_16x16x32_f16 v[42:45], v[90:93], v[46:49], v[42:45]
	v_mfma_f32_16x16x32_f16 v[38:41], v[90:93], v[50:53], v[38:41]
	v_mfma_f32_16x16x32_f16 v[6:9], v[94:97], v[46:49], v[6:9]
	v_mfma_f32_16x16x32_f16 v[2:5], v[94:97], v[50:53], v[2:5]
	ds_read_b128 v[90:93], v70 offset:37760
	ds_read_b128 v[46:49], v75
	ds_read_b128 v[50:53], v75 offset:1024
	ds_read_b128 v[94:97], v70 offset:38784
	s_waitcnt lgkmcnt(4)
	v_mfma_f32_16x16x32_f16 v[42:45], v[106:109], v[98:101], v[42:45]
	v_mfma_f32_16x16x32_f16 v[38:41], v[106:109], v[102:105], v[38:41]
	v_mfma_f32_16x16x32_f16 v[6:9], v[110:113], v[98:101], v[6:9]
	v_mfma_f32_16x16x32_f16 v[2:5], v[110:113], v[102:105], v[2:5]
	ds_read_b128 v[106:109], v70 offset:39808
	ds_read_b128 v[98:101], v74
	ds_read_b128 v[102:105], v74 offset:1024
	ds_read_b128 v[110:113], v70 offset:40832
	s_waitcnt lgkmcnt(4)
	v_mfma_f32_16x16x32_f16 v[42:45], v[90:93], v[46:49], v[42:45]
	v_mfma_f32_16x16x32_f16 v[38:41], v[90:93], v[50:53], v[38:41]
	v_mfma_f32_16x16x32_f16 v[6:9], v[94:97], v[46:49], v[6:9]
	v_mfma_f32_16x16x32_f16 v[2:5], v[94:97], v[50:53], v[2:5]
	ds_read_b128 v[90:93], v70 offset:41856
	ds_read_b128 v[46:49], v73
	ds_read_b128 v[50:53], v73 offset:1024
	ds_read_b128 v[94:97], v70 offset:42880
	s_waitcnt lgkmcnt(4)
	v_mfma_f32_16x16x32_f16 v[42:45], v[106:109], v[98:101], v[42:45]
	v_mfma_f32_16x16x32_f16 v[38:41], v[106:109], v[102:105], v[38:41]
	v_mfma_f32_16x16x32_f16 v[6:9], v[110:113], v[98:101], v[6:9]
	v_mfma_f32_16x16x32_f16 v[2:5], v[110:113], v[102:105], v[2:5]
	ds_read_b128 v[106:109], v70 offset:43904
	ds_read_b128 v[98:101], v72
	ds_read_b128 v[102:105], v72 offset:1024
	ds_read_b128 v[110:113], v70 offset:44928
	s_waitcnt lgkmcnt(4)
	v_mfma_f32_16x16x32_f16 v[42:45], v[90:93], v[46:49], v[42:45]
	v_mfma_f32_16x16x32_f16 v[38:41], v[90:93], v[50:53], v[38:41]
	v_mfma_f32_16x16x32_f16 v[6:9], v[94:97], v[46:49], v[6:9]
	v_mfma_f32_16x16x32_f16 v[2:5], v[94:97], v[50:53], v[2:5]
	ds_read_b128 v[90:93], v70 offset:45952
	ds_read_b128 v[46:49], v71
	ds_read_b128 v[50:53], v71 offset:1024
	ds_read_b128 v[94:97], v70 offset:46976
	s_waitcnt lgkmcnt(4)
	v_mfma_f32_16x16x32_f16 v[42:45], v[106:109], v[98:101], v[42:45]
	v_mfma_f32_16x16x32_f16 v[38:41], v[106:109], v[102:105], v[38:41]
	v_mfma_f32_16x16x32_f16 v[6:9], v[110:113], v[98:101], v[6:9]
	v_mfma_f32_16x16x32_f16 v[2:5], v[110:113], v[102:105], v[2:5]
	s_waitcnt lgkmcnt(0)
	v_mfma_f32_16x16x32_f16 v[42:45], v[90:93], v[46:49], v[42:45]
	v_mfma_f32_16x16x32_f16 v[38:41], v[90:93], v[50:53], v[38:41]
	v_mfma_f32_16x16x32_f16 v[6:9], v[94:97], v[46:49], v[6:9]
	v_mfma_f32_16x16x32_f16 v[2:5], v[94:97], v[50:53], v[2:5]
	s_branch .LBB2_56
.Lht_t1:
	ds_read_b128 v[90:93], v70 offset:29568
	ds_read_b128 v[46:49], v79
	ds_read_b128 v[50:53], v79 offset:1024
	ds_read_b128 v[106:109], v70 offset:31616
	ds_read_b128 v[98:101], v78
	ds_read_b128 v[102:105], v78 offset:1024
	s_waitcnt lgkmcnt(3)
	v_mfma_f32_16x16x32_f16 v[42:45], v[90:93], v[46:49], v[42:45]
	v_mfma_f32_16x16x32_f16 v[38:41], v[90:93], v[50:53], v[38:41]
	ds_read_b128 v[90:93], v70 offset:33664
	ds_read_b128 v[46:49], v77
	ds_read_b128 v[50:53], v77 offset:1024
	s_waitcnt lgkmcnt(3)
	v_mfma_f32_16x16x32_f16 v[42:45], v[106:109], v[98:101], v[42:45]
	v_mfma_f32_16x16x32_f16 v[38:41], v[106:109], v[102:105], v[38:41]
	ds_read_b128 v[106:109], v70 offset:35712
	ds_read_b128 v[98:101], v76
	ds_read_b128 v[102:105], v76 offset:1024
	s_waitcnt lgkmcnt(3)
	v_mfma_f32_16x16x32_f16 v[42:45], v[90:93], v[46:49], v[42:45]
	v_mfma_f32_16x16x32_f16 v[38:41], v[90:93], v[50:53], v[38:41]
	ds_read_b128 v[90:93], v70 offset:37760
	ds_read_b128 v[46:49], v75
	ds_read_b128 v[50:53], v75 offset:1024
	s_waitcnt lgkmcnt(3)
	v_mfma_f32_16x16x32_f16 v[42:45], v[106:109], v[98:101], v[42:45]
	v_mfma_f32_16x16x32_f16 v[38:41], v[106:109], v[102:105], v[38:41]
	ds_read_b128 v[106:109], v70 offset:39808
	ds_read_b128 v[98:101], v74
	ds_read_b128 v[102:105], v74 offset:1024
	s_waitcnt lgkmcnt(3)
	v_mfma_f32_16x16x32_f16 v[42:45], v[90:93], v[46:49], v[42:45]
	v_mfma_f32_16x16x32_f16 v[38:41], v[90:93], v[50:53], v[38:41]
	ds_read_b128 v[90:93], v70 offset:41856
	ds_read_b128 v[46:49], v73
	ds_read_b128 v[50:53], v73 offset:1024
	s_waitcnt lgkmcnt(3)
	v_mfma_f32_16x16x32_f16 v[42:45], v[106:109], v[98:101], v[42:45]
	v_mfma_f32_16x16x32_f16 v[38:41], v[106:109], v[102:105], v[38:41]
	ds_read_b128 v[106:109], v70 offset:43904
	ds_read_b128 v[98:101], v72
	ds_read_b128 v[102:105], v72 offset:1024
	s_waitcnt lgkmcnt(3)
	v_mfma_f32_16x16x32_f16 v[42:45], v[90:93], v[46:49], v[42:45]
	v_mfma_f32_16x16x32_f16 v[38:41], v[90:93], v[50:53], v[38:41]
	ds_read_b128 v[90:93], v70 offset:45952
	ds_read_b128 v[46:49], v71
	ds_read_b128 v[50:53], v71 offset:1024
	s_waitcnt lgkmcnt(3)
	v_mfma_f32_16x16x32_f16 v[42:45], v[106:109], v[98:101], v[42:45]
	v_mfma_f32_16x16x32_f16 v[38:41], v[106:109], v[102:105], v[38:41]
	s_waitcnt lgkmcnt(0)
	v_mfma_f32_16x16x32_f16 v[42:45], v[90:93], v[46:49], v[42:45]
	v_mfma_f32_16x16x32_f16 v[38:41], v[90:93], v[50:53], v[38:41]
	s_branch .LBB2_56

	.amdhsa_kernel _Z10head_fusedPKDF16_S0_S0_PKfS2_S2_S2_S2_S2_S2_S2_Pf
		.amdhsa_group_segment_fixed_size 49152
		.amdhsa_private_segment_fixed_size 0
		.amdhsa_kernarg_size 96
		.amdhsa_user_sgpr_count 2
		.amdhsa_user_sgpr_dispatch_ptr 0
		.amdhsa_user_sgpr_queue_ptr 0
		.amdhsa_user_sgpr_kernarg_segment_ptr 1
		.amdhsa_user_sgpr_dispatch_id 0
		.amdhsa_user_sgpr_kernarg_preload_length 0
		.amdhsa_user_sgpr_kernarg_preload_offset 0
		.amdhsa_user_sgpr_private_segment_size 0
		.amdhsa_uses_dynamic_stack 0
		.amdhsa_enable_private_segment 0
		.amdhsa_system_sgpr_workgroup_id_x 1
		.amdhsa_system_sgpr_workgroup_id_y 1
		.amdhsa_system_sgpr_workgroup_id_z 0
		.amdhsa_system_sgpr_workgroup_info 0
		.amdhsa_system_vgpr_workitem_id 0
		.amdhsa_next_free_vgpr 114
		.amdhsa_next_free_sgpr 91
		.amdhsa_accum_offset 116
		.amdhsa_reserve_vcc 1
		.amdhsa_float_round_mode_32 0
		.amdhsa_float_round_mode_16_64 0
		.amdhsa_float_denorm_mode_32 3
		.amdhsa_float_denorm_mode_16_64 3
		.amdhsa_dx10_clamp 1
		.amdhsa_ieee_mode 1
		.amdhsa_fp16_overflow 0
		.amdhsa_tg_split 0
		.amdhsa_exception_fp_ieee_invalid_op 0
		.amdhsa_exception_fp_denorm_src 0
		.amdhsa_exception_fp_ieee_div_zero 0
		.amdhsa_exception_fp_ieee_overflow 0
		.amdhsa_exception_fp_ieee_underflow 0
		.amdhsa_exception_fp_ieee_inexact 0
		.amdhsa_exception_int_div_zero 0
	.end_amdhsa_kernel

amdhsa.kernels:
  - .agpr_count:     0
    .args:
      - .offset:         0
        .size:           40
        .value_kind:     by_value
      - .actual_access:  read_only
        .address_space:  global
        .offset:         40
        .size:           8
        .value_kind:     global_buffer
      - .actual_access:  read_only
        .address_space:  global
        .offset:         48
        .size:           8
        .value_kind:     global_buffer
      - .actual_access:  read_only
        .address_space:  global
        .offset:         56
        .size:           8
        .value_kind:     global_buffer
      - .actual_access:  read_only
        .address_space:  global
        .offset:         64
        .size:           8
        .value_kind:     global_buffer
      - .actual_access:  read_only
        .address_space:  global
        .offset:         72
        .size:           8
        .value_kind:     global_buffer
      - .actual_access:  write_only
        .address_space:  global
        .offset:         80
        .size:           8
        .value_kind:     global_buffer
      - .actual_access:  write_only
        .address_space:  global
        .offset:         88
        .size:           8
        .value_kind:     global_buffer
      - .actual_access:  write_only
        .address_space:  global
        .offset:         96
        .size:           8
        .value_kind:     global_buffer
    .group_segment_fixed_size: 16384
    .kernarg_segment_align: 8
    .kernarg_segment_size: 104
    .language:       OpenCL C
    .language_version:
      - 2
      - 0
    .max_flat_workgroup_size: 256
    .name:           _Z8prep_all8FeatPtrsPKfS1_S1_S1_S1_PDF16_S2_S2_
    .private_segment_fixed_size: 0
    .sgpr_count:     26
    .sgpr_spill_count: 0
    .symbol:         _Z8prep_all8FeatPtrsPKfS1_S1_S1_S1_PDF16_S2_S2_.kd
    .uniform_work_group_size: 1
    .uses_dynamic_stack: false
    .vgpr_count:     38
    .vgpr_spill_count: 0
    .wavefront_size: 64
  - .agpr_count:     0
    .args:
      - .address_space:  global
        .offset:         0
        .size:           8
        .value_kind:     global_buffer
      - .address_space:  global
        .offset:         8
        .size:           8
        .value_kind:     global_buffer
      - .actual_access:  read_only
        .address_space:  global
        .offset:         16
        .size:           8
        .value_kind:     global_buffer
      - .actual_access:  write_only
        .address_space:  global
        .offset:         24
        .size:           8
        .value_kind:     global_buffer
      - .actual_access:  write_only
        .address_space:  global
        .offset:         32
        .size:           8
        .value_kind:     global_buffer
      - .offset:         40
        .size:           4
        .value_kind:     by_value
      - .offset:         44
        .size:           4
        .value_kind:     by_value
      - .address_space:  global
        .offset:         48
        .size:           8
        .value_kind:     global_buffer
      - .actual_access:  read_only
        .address_space:  global
        .offset:         56
        .size:           8
        .value_kind:     global_buffer
      - .offset:         64
        .size:           4
        .value_kind:     by_value
      - .actual_access:  read_only
        .address_space:  global
        .offset:         72
        .size:           8
        .value_kind:     global_buffer
      - .actual_access:  read_only
        .address_space:  global
        .offset:         80
        .size:           8
        .value_kind:     global_buffer
      - .offset:         88
        .size:           4
        .value_kind:     hidden_block_count_x
      - .offset:         92
        .size:           4
        .value_kind:     hidden_block_count_y
      - .offset:         96
        .size:           4
        .value_kind:     hidden_block_count_z
      - .offset:         100
        .size:           2
        .value_kind:     hidden_group_size_x
      - .offset:         102
        .size:           2
        .value_kind:     hidden_group_size_y
      - .offset:         104
        .size:           2
        .value_kind:     hidden_group_size_z
      - .offset:         106
        .size:           2
        .value_kind:     hidden_remainder_x
      - .offset:         108
        .size:           2
        .value_kind:     hidden_remainder_y
      - .offset:         110
        .size:           2
        .value_kind:     hidden_remainder_z
      - .offset:         128
        .size:           8
        .value_kind:     hidden_global_offset_x
      - .offset:         136
        .size:           8
        .value_kind:     hidden_global_offset_y
      - .offset:         144
        .size:           8
        .value_kind:     hidden_global_offset_z
      - .offset:         152
        .size:           2
        .value_kind:     hidden_grid_dims
      - .offset:         208
        .size:           4
        .value_kind:     hidden_dynamic_lds_size
    .group_segment_fixed_size: 0
    .kernarg_segment_align: 8
    .kernarg_segment_size: 344
    .language:       OpenCL C
    .language_version:
      - 2
      - 0
    .max_flat_workgroup_size: 512
    .name:           _Z9conv_gemmPKDF16_S0_PKfPDF16_PfiiS3_S2_iS2_S2_
    .private_segment_fixed_size: 0
    .sgpr_count:     78
    .sgpr_spill_count: 0
    .symbol:         _Z9conv_gemmPKDF16_S0_PKfPDF16_PfiiS3_S2_iS2_S2_.kd
    .uniform_work_group_size: 1
    .uses_dynamic_stack: false
    .vgpr_count:     256
    .vgpr_spill_count: 0
    .wavefront_size: 64
  - .agpr_count:     0
    .args:
      - .actual_access:  read_only
        .address_space:  global
        .offset:         0
        .size:           8
        .value_kind:     global_buffer
      - .actual_access:  read_only
        .address_space:  global
        .offset:         8
        .size:           8
        .value_kind:     global_buffer
      - .actual_access:  read_only
        .address_space:  global
        .offset:         16
        .size:           8
        .value_kind:     global_buffer
      - .actual_access:  read_only
        .address_space:  global
        .offset:         24
        .size:           8
        .value_kind:     global_buffer
      - .actual_access:  read_only
        .address_space:  global
        .offset:         32
        .size:           8
        .value_kind:     global_buffer
      - .actual_access:  read_only
        .address_space:  global
        .offset:         40
        .size:           8
        .value_kind:     global_buffer
      - .actual_access:  read_only
        .address_space:  global
        .offset:         48
        .size:           8
        .value_kind:     global_buffer
      - .actual_access:  read_only
        .address_space:  global
        .offset:         56
        .size:           8
        .value_kind:     global_buffer
      - .actual_access:  read_only
        .address_space:  global
        .offset:         64
        .size:           8
        .value_kind:     global_buffer
      - .actual_access:  read_only
        .address_space:  global
        .offset:         72
        .size:           8
        .value_kind:     global_buffer
      - .actual_access:  read_only
        .address_space:  global
        .offset:         80
        .size:           8
        .value_kind:     global_buffer
      - .actual_access:  write_only
        .address_space:  global
        .offset:         88
        .size:           8
        .value_kind:     global_buffer
    .group_segment_fixed_size: 49152
    .kernarg_segment_align: 8
    .kernarg_segment_size: 96
    .language:       OpenCL C
    .language_version:
      - 2
      - 0
    .max_flat_workgroup_size: 512
    .name:           _Z10head_fusedPKDF16_S0_S0_PKfS2_S2_S2_S2_S2_S2_S2_Pf
    .private_segment_fixed_size: 0
    .sgpr_count:     57
    .sgpr_spill_count: 0
    .symbol:         _Z10head_fusedPKDF16_S0_S0_PKfS2_S2_S2_S2_S2_S2_S2_Pf.kd
    .uniform_work_group_size: 1
    .uses_dynamic_stack: false
    .vgpr_count:     114
    .vgpr_spill_count: 0
    .wavefront_size: 64
